# v13 with pre-barrier L2 warm-up at 128B stride over two slices (each fragment line warmed by two blocks)
# speedup vs baseline: 1.0402x; 1.0402x over previous
.LBB2_414:
	s_movk_i32 s0, 0xc00
	v_mov_b64_e32 v[26:27], s[42:43]
	v_mul_u32_u24_e32 v28, 0xc00, v154
	v_mad_i64_i32 v[26:27], s[0:1], v62, s0, v[26:27]
	v_or_b32_e32 v28, v28, v98
	v_mov_b32_e32 v99, 0
	v_lshl_add_u64 v[26:27], v[26:27], 0, v[98:99]
	v_or_b32_e32 v29, 0x10000, v28
	global_store_dwordx4 v[26:27], v[22:25], off sc1
	ds_write_b128 v29, v[22:25]
	v_sub_f32_e32 v10, v10, v22
	v_or_b32_e32 v22, v101, v154
	v_sub_f32_e32 v11, v11, v23
	v_add_u32_e32 v23, v22, v102
	v_lshl_or_b32 v23, v23, 4, v103
	ds_write_b32 v23, v10
	v_add_u32_e32 v10, v22, v104
	v_lshl_or_b32 v10, v10, 4, v105
	ds_write_b32 v10, v11
	v_or_b32_e32 v10, v106, v154
	v_add_u32_e32 v10, v10, v107
	v_sub_f32_e32 v12, v12, v24
	v_lshl_or_b32 v10, v10, 4, v108
	ds_write_b32 v10, v12
	v_or_b32_e32 v10, v109, v154
	v_add_u32_e32 v10, v10, v110
	v_sub_f32_e32 v13, v13, v25
	v_lshl_or_b32 v10, v10, 4, v111
	ds_write_b32 v10, v13
	v_add_u32_e32 v10, 0x10400, v28
	ds_write_b128 v10, v[18:21]
	v_sub_f32_e32 v10, v6, v18
	v_sub_f32_e32 v11, v7, v19
	v_pk_add_f32 v[6:7], v[8:9], v[20:21] neg_lo:[0,1] neg_hi:[0,1]
	v_or_b32_e32 v8, v112, v154
	v_add_u32_e32 v9, v8, v113
	v_add_u32_e32 v8, v8, v115
	v_lshl_or_b32 v9, v9, 4, v114
	v_lshl_or_b32 v8, v8, 4, v116
	ds_write_b32 v9, v10
	ds_write_b32 v8, v11
	v_or_b32_e32 v8, v117, v154
	v_add_u32_e32 v8, v8, v118
	v_lshl_or_b32 v8, v8, 4, v119
	ds_write_b32 v8, v6
	v_or_b32_e32 v6, v120, v154
	v_add_u32_e32 v6, v6, v121
	v_lshl_or_b32 v6, v6, 4, v122
	ds_write_b32 v6, v7
	v_add_u32_e32 v6, 0x10800, v28
	ds_write_b128 v6, v[14:17]
	v_or_b32_e32 v6, v123, v154
	v_add_u32_e32 v7, v6, v124
	v_pk_add_f32 v[2:3], v[2:3], v[14:15] neg_lo:[0,1] neg_hi:[0,1]
	v_lshl_or_b32 v7, v7, 4, v125
	ds_write_b32 v7, v2
	v_add_u32_e32 v2, v6, v126
	v_lshl_or_b32 v2, v2, 4, v127
	ds_write_b32 v2, v3
	v_or_b32_e32 v2, v133, v154
	v_add_u32_e32 v2, v2, v134
	v_pk_add_f32 v[4:5], v[4:5], v[16:17] neg_lo:[0,1] neg_hi:[0,1]
	v_lshl_or_b32 v2, v2, 4, v63
	ds_write_b32 v2, v4
	v_or_b32_e32 v2, v135, v154
	v_add_u32_e32 v2, v2, v132
	v_lshl_or_b32 v2, v2, 4, v136
	v_add_lshl_u32 v4, v100, v154, 4
	s_mov_b32 s5, 0
	s_mov_b32 s4, 1.0
	ds_write_b32 v2, v5
	v_mov_b64_e32 v[2:3], s[4:5]
	v_add_u32_e32 v4, 8, v4
	s_waitcnt vmcnt(1)
	v_lshlrev_b32_e32 v40, 9, v150
	ds_write2st64_b64 v4, v[2:3], v[2:3] offset1:64
	v_or_b32_e32 v2, v40, v128
	v_lshlrev_b32_e32 v98, 4, v2
	v_lshl_add_u64 v[100:101], s[40:41], 0, v[98:99]
	s_mov_b64 s[0:1], 0x787000
	v_lshl_add_u64 v[34:35], v[100:101], 0, s[0:1]
	s_mov_b32 s0, 0x788000
	v_add_co_u32_e32 v36, vcc, s0, v100
	global_store_dwordx4 v[26:27], v[18:21], off offset:1024 sc1
	global_store_dwordx4 v[26:27], v[14:17], off offset:2048 sc1
	s_lshr_b32 s59, s33, 4
	s_and_b32 s59, s59, 31
	s_lshl_b32 s59, s59, 15
	s_add_u32 s59, s59, 0x787000
	s_add_u32 s68, s40, s59
	s_addc_u32 s69, s41, 0
	v_lshlrev_b32_e32 v207, 7, v0
	global_load_dword v207, v207, s[68:69]
	s_waitcnt lgkmcnt(0)
	s_barrier
	v_addc_co_u32_e32 v37, vcc, 0, v101, vcc
	global_load_dwordx4 v[2:5], v[34:35], off offset:1024
	global_load_dwordx4 v[10:13], v[34:35], off offset:2048
	global_load_dwordx4 v[14:17], v[34:35], off offset:3072
	global_load_dwordx4 v[6:9], v[36:37], off offset:-4096
	global_load_dwordx4 v[18:21], v[36:37], off
	global_load_dwordx4 v[22:25], v[36:37], off offset:1024
	global_load_dwordx4 v[26:29], v[36:37], off offset:2048
	global_load_dwordx4 v[30:33], v[36:37], off offset:3072
	v_and_b32_e32 v35, 15, v0
	v_lshrrev_b32_e32 v37, 4, v128
	v_lshlrev_b32_e32 v102, 2, v35
	v_lshlrev_b32_e32 v41, 2, v37
	v_lshlrev_b32_e32 v34, 4, v35
	v_cmp_gt_u32_e64 s[0:1], 6, v35
	v_mov_b32_e32 v35, v99
	v_or3_b32 v36, v34, v41, v40
	v_lshl_add_u64 v[104:105], s[44:45], 0, v[34:35]
	v_or_b32_e32 v34, v40, v34
	s_movk_i32 s4, 0x1000
	v_or3_b32 v153, v34, v41, s4
	v_or_b32_e32 v34, 0x11800, v98
	v_lshl_add_u64 v[118:119], s[40:41], 0, v[34:35]
	v_or_b32_e32 v34, 0x11400, v98
	v_lshl_add_u64 v[120:121], s[40:41], 0, v[34:35]
	v_or_b32_e32 v34, 0x11000, v98
	ds_read2st64_b32 v[132:133], v36 offset1:1
	v_or_b32_e32 v36, s33, v41
	v_lshl_add_u64 v[122:123], s[40:41], 0, v[34:35]
	v_or_b32_e32 v34, 0x10c00, v98
	v_or_b32_e32 v38, 1, v36
	v_lshl_add_u64 v[124:125], s[40:41], 0, v[34:35]
	v_or_b32_e32 v34, 0x10800, v98
	v_mul_u32_u24_e32 v152, 0x3000, v37
	v_ashrrev_i32_e32 v37, 31, v36
	v_ashrrev_i32_e32 v39, 31, v38
	v_lshl_add_u64 v[126:127], s[40:41], 0, v[34:35]
	v_or_b32_e32 v34, 0x10400, v98
	v_mov_b32_e32 v103, v99
	v_lshlrev_b64 v[108:109], 17, v[36:37]
	v_lshlrev_b64 v[110:111], 17, v[38:39]
	v_or_b32_e32 v38, 2, v36
	v_or_b32_e32 v36, 3, v36
	v_lshl_add_u64 v[128:129], s[40:41], 0, v[34:35]
	v_mul_u32_u24_e32 v34, 24, v150
	v_lshl_add_u64 v[106:107], s[38:39], 0, v[102:103]
	v_ashrrev_i32_e32 v39, 31, v38
	v_ashrrev_i32_e32 v37, 31, v36
	v_lshlrev_b32_e32 v103, 2, v0
	v_or_b32_e32 v98, 0x11c00, v98
	v_or_b32_e32 v34, v152, v34
	v_lshlrev_b64 v[112:113], 17, v[38:39]
	v_lshlrev_b64 v[114:115], 17, v[36:37]
	v_and_b32_e32 v116, 0x700, v103
	v_mov_b32_e32 v117, v99
	v_lshl_add_u64 v[130:131], s[40:41], 0, v[98:99]
	v_add_u32_e32 v154, v34, v102
	s_mov_b64 s[6:7], 0
	s_mov_b64 s[8:9], 0x800
	v_mov_b32_e32 v155, 0x400
	v_mov_b32_e32 v159, 0
	v_mov_b32_e32 v158, 0
	v_mov_b32_e32 v157, 0
	v_mov_b32_e32 v156, 0
	v_readfirstlane_b32 s78, v150
	v_and_b32_e32 v104, 63, v0
	v_lshlrev_b32_e32 v104, 4, v104
	v_lshl_or_b32 v104, v150, 13, v104
	v_add_u32_e32 v105, 0xfffff000, v153
	v_mov_b32_e32 v106, v154
	v_lshrrev_b32_e32 v98, 2, v102
	v_cmp_gt_u32_e32 vcc, 6, v98
	v_add_u32_e32 v107, -6, v98
	s_nop 0
	v_cndmask_b32_e32 v107, v107, v98, vcc
	v_cmp_gt_u32_e32 vcc, 6, v107
	v_add_u32_e32 v98, -6, v107
	s_nop 0
	v_cndmask_b32_e32 v107, v98, v107, vcc
	v_lshlrev_b32_e32 v107, 2, v107
	v_sub_u32_e32 v106, v106, v102
	v_add_u32_e32 v106, v106, v107
	v_and_b32_e32 v98, 63, v0
	v_lshrrev_b32_e32 v98, 4, v98
	v_lshlrev_b32_e32 v98, 19, v98
	v_lshl_or_b32 v108, v102, 2, v98
	v_add_u32_e32 v109, 0x20000, v108
	v_add_u32_e32 v110, 0x40000, v108
	v_add_u32_e32 v111, 0x60000, v108
	v_mov_b32_e32 v240, 0
	v_mov_b32_e32 v241, 0
	v_mov_b32_e32 v242, 0
	v_mov_b32_e32 v243, 0
	s_lshl_b32 s84, s33, 17
	s_lshl_b32 s85, s78, 10
	s_add_u32 s84, s84, s85
	s_add_u32 s80, s44, s84
	s_addc_u32 s81, s45, 0
	s_mul_i32 s84, s78, 0x1800
	s_add_u32 s94, s38, s84
	s_addc_u32 s95, s39, 0
	s_mov_b32 s70, 0
	s_add_u32 s86, s40, 0x797000
	s_addc_u32 s87, s41, 0
	s_add_u32 s88, s86, 0x1000
	s_addc_u32 s89, s87, 0
	v_add_u32_e32 v112, 0x1000, v105
	s_waitcnt vmcnt(0) lgkmcnt(0)
	v_mfma_f32_16x16x4_f32 v[34:37], v132, v6, 0
	v_mfma_f32_16x16x4_f32 v[38:41], v132, v8, 0
	v_mfma_f32_16x16x4_f32 v[34:37], v133, v7, v[34:37]
	v_mfma_f32_16x16x4_f32 v[38:41], v133, v9, v[38:41]
	global_load_dwordx4 v[6:9], v104, s[86:87]
	v_mfma_f32_16x16x4_f32 v[42:45], v132, v2, 0
	v_mfma_f32_16x16x4_f32 v[46:49], v132, v4, 0
	v_mfma_f32_16x16x4_f32 v[42:45], v133, v3, v[42:45]
	v_mfma_f32_16x16x4_f32 v[46:49], v133, v5, v[46:49]
	global_load_dwordx4 v[2:5], v104, s[86:87] offset:1024
	v_mfma_f32_16x16x4_f32 v[50:53], v132, v10, 0
	v_mfma_f32_16x16x4_f32 v[54:57], v132, v12, 0
	v_mfma_f32_16x16x4_f32 v[50:53], v133, v11, v[50:53]
	v_mfma_f32_16x16x4_f32 v[54:57], v133, v13, v[54:57]
	global_load_dwordx4 v[10:13], v104, s[86:87] offset:2048
	v_mfma_f32_16x16x4_f32 v[58:61], v132, v14, 0
	v_mfma_f32_16x16x4_f32 v[62:65], v132, v16, 0
	v_mfma_f32_16x16x4_f32 v[58:61], v133, v15, v[58:61]
	v_mfma_f32_16x16x4_f32 v[62:65], v133, v17, v[62:65]
	global_load_dwordx4 v[14:17], v104, s[86:87] offset:3072
	v_mfma_f32_16x16x4_f32 v[66:69], v132, v18, 0
	v_mfma_f32_16x16x4_f32 v[70:73], v132, v20, 0
	v_mfma_f32_16x16x4_f32 v[66:69], v133, v19, v[66:69]
	v_mfma_f32_16x16x4_f32 v[70:73], v133, v21, v[70:73]
	global_load_dwordx4 v[18:21], v104, s[88:89]
	v_mfma_f32_16x16x4_f32 v[74:77], v132, v22, 0
	v_mfma_f32_16x16x4_f32 v[78:81], v132, v24, 0
	v_mfma_f32_16x16x4_f32 v[74:77], v133, v23, v[74:77]
	v_mfma_f32_16x16x4_f32 v[78:81], v133, v25, v[78:81]
	global_load_dwordx4 v[22:25], v104, s[88:89] offset:1024
	v_mfma_f32_16x16x4_f32 v[82:85], v132, v26, 0
	v_mfma_f32_16x16x4_f32 v[86:89], v132, v28, 0
	v_mfma_f32_16x16x4_f32 v[82:85], v133, v27, v[82:85]
	v_mfma_f32_16x16x4_f32 v[86:89], v133, v29, v[86:89]
	global_load_dwordx4 v[26:29], v104, s[88:89] offset:2048
	v_mfma_f32_16x16x4_f32 v[90:93], v132, v30, 0
	v_mfma_f32_16x16x4_f32 v[94:97], v132, v32, 0
	v_mfma_f32_16x16x4_f32 v[90:93], v133, v31, v[90:93]
	v_mfma_f32_16x16x4_f32 v[94:97], v133, v33, v[94:97]
	global_load_dwordx4 v[30:33], v104, s[88:89] offset:3072
	ds_read2st64_b32 v[132:133], v112 offset1:1
	s_nop 7
	s_nop 7
	v_max3_f32 v114, v34, v38, v42
	v_max3_f32 v116, v46, v50, v54
	v_max3_f32 v114, v114, v58, v62
	v_max3_f32 v116, v116, v66, v70
	v_max3_f32 v114, v114, v74, v78
	v_max3_f32 v116, v116, v82, v86
	v_max3_f32 v114, v114, v90, v94
	v_max_f32_e32 v114, v114, v116
	s_nop 1
	v_max_f32_dpp v114, v114, v114 row_ror:1 row_mask:0xf bank_mask:0xf
	s_nop 1
	v_max_f32_dpp v114, v114, v114 row_ror:2 row_mask:0xf bank_mask:0xf
	s_nop 1
	v_max_f32_dpp v114, v114, v114 row_ror:4 row_mask:0xf bank_mask:0xf
	s_nop 1
	v_max_f32_dpp v114, v114, v114 row_ror:8 row_mask:0xf bank_mask:0xf
	s_waitcnt vmcnt(0) lgkmcnt(0)
